# attention PV: 16 transition lgkmcnt(0) waits moved behind the next MFMA whose operands were already covered
# speedup vs baseline: 1.0082x; 1.0082x over previous
; #define AT_SBAR() __builtin_amdgcn_sched_barrier(0)
; template <int OFF> DI s16x4 tr_read(int vb) { s16x4 r; asm volatile("ds_read_b64_tr_b16 %0, %1 offset:%2" : "=&v"(r) : "v"(vb), "i"(OFF) : "memory"); return r; }
; template <int D0> DI void pv_one(f32x16& od, int vb, bf16x8 pa0, bf16x8 pa1, bf16x8 pa2, bf16x8 pa3) {
;     const s16x4 l0 = tr_read<v_rd_off(D0, 0, 0)>(vb), h0 = tr_read<v_rd_off(D0, 0, 1)>(vb), l1 = tr_read<v_rd_off(D0, 1, 0)>(vb), h1 = tr_read<v_rd_off(D0, 1, 1)>(vb);
;     const s16x4 l2 = tr_read<v_rd_off(D0, 2, 0)>(vb), h2 = tr_read<v_rd_off(D0, 2, 1)>(vb), l3 = tr_read<v_rd_off(D0, 3, 0)>(vb), h3 = tr_read<v_rd_off(D0, 3, 1)>(vb);
;     asm volatile("s_waitcnt lgkmcnt(0)" ::: "memory"); AT_SBAR();
;     ...
;     od = __builtin_amdgcn_mfma_f32_32x32x16_bf16(AT_PK(l0, h0), pa0, od, 0, 0, 0);
;     od = __builtin_amdgcn_mfma_f32_32x32x16_bf16(AT_PK(l1, h1), pa1, od, 0, 0, 0);
;     od = __builtin_amdgcn_mfma_f32_32x32x16_bf16(AT_PK(l2, h2), pa2, od, 0, 0, 0);
;     od = __builtin_amdgcn_mfma_f32_32x32x16_bf16(AT_PK(l3, h3), pa3, od, 0, 0, 0);
;     ...
; }
; DI void pv_all_sm(f32x16* o, int vb, bf16x8 pa0, bf16x8 pa1, bf16x8 pa2, bf16x8 pa3, f32x16& p0, f32x16& p1, float& m_ref, f32x16& negm, float& alpha) {
;     pv_one<0>(o[0], vb, pa0, pa1, pa2, pa3);
;     float pmax = p0[0];
; #pragma unroll
;     for (int r = 1; r < 16; ++r) pmax = fmaxf(pmax, p0[r]);
;     pv_one<1>(o[1], vb, pa0, pa1, pa2, pa3);
; #pragma unroll
;     for (int r = 0; r < 16; ++r) pmax = fmaxf(pmax, p1[r]);
;     { auto rr = __builtin_amdgcn_permlane32_swap(__float_as_uint(pmax), __float_as_uint(pmax), false, false); pmax = fmaxf(__uint_as_float(rr[0]), __uint_as_float(rr[1])); }
;     pv_one<2>(o[2], vb, pa0, pa1, pa2, pa3);
;     alpha = 1.f;
;     if (__builtin_expect(!__all(pmax <= THRL), 0)) {
;         const float dl = fmaxf(pmax, 0.f); m_ref += dl; alpha = __builtin_amdgcn_exp2f(-dl);
; #pragma unroll
;         for (int r = 0; r < 16; ++r) { p0[r] -= dl; p1[r] -= dl; }
; #pragma unroll
;         for (int r = 0; r < 16; ++r) negm[r] = -m_ref;
;     }
.LBB4_704:
	s_lshl_b32 s67, s65, 14
	v_add_u32_e32 v186, s67, v253
	ds_read_b64_tr_b16 v[64:65], v186 offset:0
	ds_read_b64_tr_b16 v[66:67], v186 offset:0x100
	ds_read_b64_tr_b16 v[68:69], v186 offset:0x1000
	ds_read_b64_tr_b16 v[70:71], v186 offset:0x1100
	ds_read_b64_tr_b16 v[72:73], v186 offset:0x2000
	ds_read_b64_tr_b16 v[74:75], v186 offset:0x2100
	ds_read_b64_tr_b16 v[76:77], v186 offset:0x3000
	ds_read_b64_tr_b16 v[78:79], v186 offset:0x3100
	s_waitcnt lgkmcnt(0)
	s_nop 0
	v_mfma_f32_32x32x16_bf16 v[32:47], v[64:67], v[96:99], v[32:47]
	v_max_f32_e32 v64, v128, v129
	v_max3_f32 v64, v64, v130, v131
	v_max3_f32 v64, v64, v132, v133
	v_max3_f32 v64, v64, v134, v135
	v_max3_f32 v64, v64, v136, v137
	v_mfma_f32_32x32x16_bf16 v[32:47], v[68:71], v[108:111], v[32:47]
	v_max3_f32 v64, v64, v138, v139
	v_max3_f32 v66, v64, v140, v141
	ds_read_b64_tr_b16 v[64:65], v186 offset:0x200
	v_max3_f32 v180, v66, v142, v143
	ds_read_b64_tr_b16 v[66:67], v186 offset:0x300
	ds_read_b64_tr_b16 v[68:69], v186 offset:0x1200
	ds_read_b64_tr_b16 v[70:71], v186 offset:0x1300
	v_mfma_f32_32x32x16_bf16 v[32:47], v[72:75], v[100:103], v[32:47]
	ds_read_b64_tr_b16 v[72:73], v186 offset:0x2200
	ds_read_b64_tr_b16 v[74:75], v186 offset:0x2300
	ds_read_b64_tr_b16 v[214:215], v186 offset:0x3200
	ds_read_b64_tr_b16 v[216:217], v186 offset:0x3300
	v_mfma_f32_32x32x16_bf16 v[32:47], v[76:79], v[104:107], v[32:47]
	s_waitcnt lgkmcnt(0)
	v_mfma_f32_32x32x16_bf16 v[48:63], v[64:67], v[96:99], v[48:63]
	v_max3_f32 v76, v180, v112, v113
	v_max3_f32 v64, v76, v114, v115
	ds_read_b64_tr_b16 v[66:67], v186 offset:0x400
	v_max3_f32 v64, v64, v116, v117
	v_max3_f32 v64, v64, v118, v119
	v_max3_f32 v64, v64, v120, v121
	v_max3_f32 v64, v64, v122, v123
	v_mfma_f32_32x32x16_bf16 v[48:63], v[68:71], v[108:111], v[48:63]
	ds_read_b64_tr_b16 v[68:69], v186 offset:0x500
	ds_read_b64_tr_b16 v[70:71], v186 offset:0x1400
	v_max3_f32 v64, v64, v124, v125
	v_max3_f32 v64, v64, v126, v127
	v_mov_b32_e32 v65, v64
	s_nop 1
	v_permlane32_swap_b32_e32 v64, v65
	v_mfma_f32_32x32x16_bf16 v[48:63], v[72:75], v[100:103], v[48:63]
	ds_read_b64_tr_b16 v[72:73], v186 offset:0x1500
	ds_read_b64_tr_b16 v[74:75], v186 offset:0x2400
	ds_read_b64_tr_b16 v[76:77], v186 offset:0x2500
	ds_read_b64_tr_b16 v[218:219], v186 offset:0x3400
	ds_read_b64_tr_b16 v[220:221], v186 offset:0x3500
	v_mfma_f32_32x32x16_bf16 v[48:63], v[214:217], v[104:107], v[48:63]
	s_waitcnt lgkmcnt(0)
	v_max_f32_e32 v64, v64, v65
	v_mfma_f32_32x32x16_bf16 v[16:31], v[66:69], v[96:99], v[16:31]
	v_cmp_ge_f32_e32 vcc, s25, v64
	s_cmp_eq_u64 vcc, exec
	v_mfma_f32_32x32x16_bf16 v[16:31], v[70:73], v[108:111], v[16:31]
	v_mfma_f32_32x32x16_bf16 v[16:31], v[74:77], v[100:103], v[16:31]
	v_mfma_f32_32x32x16_bf16 v[16:31], v[218:221], v[104:107], v[16:31]
	s_cbranch_scc0 .LBB4_737
	v_mov_b32_e32 v180, 1.0

; #define AT_SBAR() __builtin_amdgcn_sched_barrier(0)
; template <int OFF> DI s16x4 tr_read(int vb) { s16x4 r; asm volatile("ds_read_b64_tr_b16 %0, %1 offset:%2" : "=&v"(r) : "v"(vb), "i"(OFF) : "memory"); return r; }
; template <int D0> DI void pv_one(f32x16& od, int vb, bf16x8 pa0, bf16x8 pa1, bf16x8 pa2, bf16x8 pa3) {
;     const s16x4 l0 = tr_read<v_rd_off(D0, 0, 0)>(vb), h0 = tr_read<v_rd_off(D0, 0, 1)>(vb), l1 = tr_read<v_rd_off(D0, 1, 0)>(vb), h1 = tr_read<v_rd_off(D0, 1, 1)>(vb);
;     const s16x4 l2 = tr_read<v_rd_off(D0, 2, 0)>(vb), h2 = tr_read<v_rd_off(D0, 2, 1)>(vb), l3 = tr_read<v_rd_off(D0, 3, 0)>(vb), h3 = tr_read<v_rd_off(D0, 3, 1)>(vb);
;     asm volatile("s_waitcnt lgkmcnt(0)" ::: "memory"); AT_SBAR();
;     ...
;     od = __builtin_amdgcn_mfma_f32_32x32x16_bf16(AT_PK(l0, h0), pa0, od, 0, 0, 0);
;     od = __builtin_amdgcn_mfma_f32_32x32x16_bf16(AT_PK(l1, h1), pa1, od, 0, 0, 0);
;     od = __builtin_amdgcn_mfma_f32_32x32x16_bf16(AT_PK(l2, h2), pa2, od, 0, 0, 0);
;     od = __builtin_amdgcn_mfma_f32_32x32x16_bf16(AT_PK(l3, h3), pa3, od, 0, 0, 0);
;     ...
; }
; DI void pv_all_sm(f32x16* o, int vb, bf16x8 pa0, bf16x8 pa1, bf16x8 pa2, bf16x8 pa3, f32x16& p0, f32x16& p1, float& m_ref, f32x16& negm, float& alpha) {
;     pv_one<0>(o[0], vb, pa0, pa1, pa2, pa3);
;     float pmax = p0[0];
; #pragma unroll
;     for (int r = 1; r < 16; ++r) pmax = fmaxf(pmax, p0[r]);
;     pv_one<1>(o[1], vb, pa0, pa1, pa2, pa3);
; #pragma unroll
;     for (int r = 0; r < 16; ++r) pmax = fmaxf(pmax, p1[r]);
;     { auto rr = __builtin_amdgcn_permlane32_swap(__float_as_uint(pmax), __float_as_uint(pmax), false, false); pmax = fmaxf(__uint_as_float(rr[0]), __uint_as_float(rr[1])); }
;     pv_one<2>(o[2], vb, pa0, pa1, pa2, pa3);
;     alpha = 1.f;
;     if (__builtin_expect(!__all(pmax <= THRL), 0)) {
;         const float dl = fmaxf(pmax, 0.f); m_ref += dl; alpha = __builtin_amdgcn_exp2f(-dl);
; #pragma unroll
;         for (int r = 0; r < 16; ++r) { p0[r] -= dl; p1[r] -= dl; }
; #pragma unroll
;         for (int r = 0; r < 16; ++r) negm[r] = -m_ref;
;     }
.LBB4_725:
	v_lshl_add_u32 v215, s66, 14, v253
	ds_read_b64_tr_b16 v[216:217], v215 offset:0
	ds_read_b64_tr_b16 v[218:219], v215 offset:0x100
	ds_read_b64_tr_b16 v[220:221], v215 offset:0x1000
	ds_read_b64_tr_b16 v[222:223], v215 offset:0x1100
	ds_read_b64_tr_b16 v[224:225], v215 offset:0x2000
	ds_read_b64_tr_b16 v[226:227], v215 offset:0x2100
	ds_read_b64_tr_b16 v[228:229], v215 offset:0x3000
	ds_read_b64_tr_b16 v[230:231], v215 offset:0x3100
	s_waitcnt lgkmcnt(0)
	s_nop 0
	v_mfma_f32_32x32x16_bf16 v[32:47], v[216:219], v[120:123], v[32:47]
	v_max_f32_e32 v186, v128, v129
	ds_read_b64_tr_b16 v[216:217], v215 offset:0x200
	ds_read_b64_tr_b16 v[218:219], v215 offset:0x300
	v_max3_f32 v186, v186, v130, v131
	v_max3_f32 v186, v186, v132, v133
	v_mfma_f32_32x32x16_bf16 v[32:47], v[220:223], v[124:127], v[32:47]
	ds_read_b64_tr_b16 v[220:221], v215 offset:0x1200
	ds_read_b64_tr_b16 v[222:223], v215 offset:0x1300
	v_max3_f32 v186, v186, v134, v135
	v_max3_f32 v186, v186, v136, v137
	v_max3_f32 v186, v186, v138, v139
	v_max3_f32 v186, v186, v140, v141
	v_max3_f32 v186, v186, v142, v143
	v_mfma_f32_32x32x16_bf16 v[32:47], v[224:227], v[112:115], v[32:47]
	ds_read_b64_tr_b16 v[224:225], v215 offset:0x2200
	ds_read_b64_tr_b16 v[226:227], v215 offset:0x2300
	ds_read_b64_tr_b16 v[232:233], v215 offset:0x3200
	ds_read_b64_tr_b16 v[234:235], v215 offset:0x3300
	v_mfma_f32_32x32x16_bf16 v[32:47], v[228:231], v[116:119], v[32:47]
	s_waitcnt lgkmcnt(0)
	v_mfma_f32_32x32x16_bf16 v[48:63], v[216:219], v[120:123], v[48:63]
	v_max3_f32 v186, v186, v96, v97
	v_max3_f32 v186, v186, v98, v99
	ds_read_b64_tr_b16 v[218:219], v215 offset:0x400
	v_max3_f32 v186, v186, v100, v101
	v_max3_f32 v186, v186, v102, v103
	v_max3_f32 v186, v186, v104, v105
	v_max3_f32 v186, v186, v106, v107
	v_mfma_f32_32x32x16_bf16 v[48:63], v[220:223], v[124:127], v[48:63]
	ds_read_b64_tr_b16 v[220:221], v215 offset:0x500
	ds_read_b64_tr_b16 v[222:223], v215 offset:0x1400
	v_max3_f32 v186, v186, v108, v109
	v_max3_f32 v186, v186, v110, v111
	v_mov_b32_e32 v216, v186
	s_nop 1
	v_permlane32_swap_b32_e32 v186, v216
	v_mfma_f32_32x32x16_bf16 v[48:63], v[224:227], v[112:115], v[48:63]
	ds_read_b64_tr_b16 v[224:225], v215 offset:0x1500
	ds_read_b64_tr_b16 v[226:227], v215 offset:0x2400
	ds_read_b64_tr_b16 v[228:229], v215 offset:0x2500
	ds_read_b64_tr_b16 v[236:237], v215 offset:0x3400
	ds_read_b64_tr_b16 v[238:239], v215 offset:0x3500
	v_mfma_f32_32x32x16_bf16 v[48:63], v[232:235], v[116:119], v[48:63]
	s_waitcnt lgkmcnt(0)
	v_max_f32_e32 v216, v186, v216
	v_mfma_f32_32x32x16_bf16 v[16:31], v[218:221], v[120:123], v[16:31]
	v_cmp_ge_f32_e32 vcc, s25, v216
	s_cmp_eq_u64 vcc, exec
	v_mov_b32_e32 v186, 1.0
	v_mfma_f32_32x32x16_bf16 v[16:31], v[222:225], v[124:127], v[16:31]
	v_mfma_f32_32x32x16_bf16 v[16:31], v[226:229], v[112:115], v[16:31]
	v_mfma_f32_32x32x16_bf16 v[16:31], v[236:239], v[116:119], v[16:31]
	s_cbranch_scc0 .LBB4_738

; #define AT_SBAR() __builtin_amdgcn_sched_barrier(0)
; template <int OFF> DI s16x4 tr_read(int vb) { s16x4 r; asm volatile("ds_read_b64_tr_b16 %0, %1 offset:%2" : "=&v"(r) : "v"(vb), "i"(OFF) : "memory"); return r; }
; template <int D0> DI void pv_one(f32x16& od, int vb, bf16x8 pa0, bf16x8 pa1, bf16x8 pa2, bf16x8 pa3) {
;     const s16x4 l0 = tr_read<v_rd_off(D0, 0, 0)>(vb), h0 = tr_read<v_rd_off(D0, 0, 1)>(vb), l1 = tr_read<v_rd_off(D0, 1, 0)>(vb), h1 = tr_read<v_rd_off(D0, 1, 1)>(vb);
;     const s16x4 l2 = tr_read<v_rd_off(D0, 2, 0)>(vb), h2 = tr_read<v_rd_off(D0, 2, 1)>(vb), l3 = tr_read<v_rd_off(D0, 3, 0)>(vb), h3 = tr_read<v_rd_off(D0, 3, 1)>(vb);
;     asm volatile("s_waitcnt lgkmcnt(0)" ::: "memory"); AT_SBAR();
;     ...
;     od = __builtin_amdgcn_mfma_f32_32x32x16_bf16(AT_PK(l0, h0), pa0, od, 0, 0, 0);
;     od = __builtin_amdgcn_mfma_f32_32x32x16_bf16(AT_PK(l1, h1), pa1, od, 0, 0, 0);
;     od = __builtin_amdgcn_mfma_f32_32x32x16_bf16(AT_PK(l2, h2), pa2, od, 0, 0, 0);
;     od = __builtin_amdgcn_mfma_f32_32x32x16_bf16(AT_PK(l3, h3), pa3, od, 0, 0, 0);
;     ...
; }
; DI void pv_all_sm(f32x16* o, int vb, bf16x8 pa0, bf16x8 pa1, bf16x8 pa2, bf16x8 pa3, f32x16& p0, f32x16& p1, float& m_ref, f32x16& negm, float& alpha) {
;     pv_one<0>(o[0], vb, pa0, pa1, pa2, pa3);
;     float pmax = p0[0];
; #pragma unroll
;     for (int r = 1; r < 16; ++r) pmax = fmaxf(pmax, p0[r]);
;     pv_one<1>(o[1], vb, pa0, pa1, pa2, pa3);
; #pragma unroll
;     for (int r = 0; r < 16; ++r) pmax = fmaxf(pmax, p1[r]);
;     { auto rr = __builtin_amdgcn_permlane32_swap(__float_as_uint(pmax), __float_as_uint(pmax), false, false); pmax = fmaxf(__uint_as_float(rr[0]), __uint_as_float(rr[1])); }
;     pv_one<2>(o[2], vb, pa0, pa1, pa2, pa3);
;     alpha = 1.f;
;     if (__builtin_expect(!__all(pmax <= THRL), 0)) {
;         const float dl = fmaxf(pmax, 0.f); m_ref += dl; alpha = __builtin_amdgcn_exp2f(-dl);
; #pragma unroll
;         for (int r = 0; r < 16; ++r) { p0[r] -= dl; p1[r] -= dl; }
; #pragma unroll
;         for (int r = 0; r < 16; ++r) negm[r] = -m_ref;
;     }
.LBB4_777:
	s_lshl_b32 s31, s29, 14
	v_add_u32_e32 v182, s31, v253
	ds_read_b64_tr_b16 v[64:65], v182 offset:0
	ds_read_b64_tr_b16 v[66:67], v182 offset:0x100
	ds_read_b64_tr_b16 v[68:69], v182 offset:0x1000
	ds_read_b64_tr_b16 v[70:71], v182 offset:0x1100
	ds_read_b64_tr_b16 v[72:73], v182 offset:0x2000
	ds_read_b64_tr_b16 v[74:75], v182 offset:0x2100
	ds_read_b64_tr_b16 v[76:77], v182 offset:0x3000
	ds_read_b64_tr_b16 v[78:79], v182 offset:0x3100
	s_waitcnt lgkmcnt(0)
	s_nop 0
	v_mfma_f32_32x32x16_bf16 v[48:63], v[64:67], v[96:99], v[48:63]
	v_max_f32_e32 v64, v128, v129
	v_max3_f32 v64, v64, v130, v131
	v_max3_f32 v64, v64, v132, v133
	v_max3_f32 v64, v64, v134, v135
	v_max3_f32 v64, v64, v136, v137
	v_mfma_f32_32x32x16_bf16 v[48:63], v[68:71], v[108:111], v[48:63]
	v_max3_f32 v64, v64, v138, v139
	v_max3_f32 v66, v64, v140, v141
	ds_read_b64_tr_b16 v[64:65], v182 offset:0x200
	v_max3_f32 v180, v66, v142, v143
	ds_read_b64_tr_b16 v[66:67], v182 offset:0x300
	ds_read_b64_tr_b16 v[68:69], v182 offset:0x1200
	ds_read_b64_tr_b16 v[70:71], v182 offset:0x1300
	v_mfma_f32_32x32x16_bf16 v[48:63], v[72:75], v[100:103], v[48:63]
	ds_read_b64_tr_b16 v[72:73], v182 offset:0x2200
	ds_read_b64_tr_b16 v[74:75], v182 offset:0x2300
	ds_read_b64_tr_b16 v[218:219], v182 offset:0x3200
	ds_read_b64_tr_b16 v[220:221], v182 offset:0x3300
	v_mfma_f32_32x32x16_bf16 v[48:63], v[76:79], v[104:107], v[48:63]
	s_waitcnt lgkmcnt(0)
	v_mfma_f32_32x32x16_bf16 v[32:47], v[64:67], v[96:99], v[32:47]
	v_max3_f32 v76, v180, v112, v113
	v_max3_f32 v64, v76, v114, v115
	ds_read_b64_tr_b16 v[66:67], v182 offset:0x400
	v_max3_f32 v64, v64, v116, v117
	v_max3_f32 v64, v64, v118, v119
	v_max3_f32 v64, v64, v120, v121
	v_max3_f32 v64, v64, v122, v123
	v_mfma_f32_32x32x16_bf16 v[32:47], v[68:71], v[108:111], v[32:47]
	ds_read_b64_tr_b16 v[68:69], v182 offset:0x500
	ds_read_b64_tr_b16 v[70:71], v182 offset:0x1400
	v_max3_f32 v64, v64, v124, v125
	v_max3_f32 v64, v64, v126, v127
	v_mov_b32_e32 v65, v64
	s_nop 1
	v_permlane32_swap_b32_e32 v64, v65
	v_mfma_f32_32x32x16_bf16 v[32:47], v[72:75], v[100:103], v[32:47]
	ds_read_b64_tr_b16 v[72:73], v182 offset:0x1500
	ds_read_b64_tr_b16 v[74:75], v182 offset:0x2400
	ds_read_b64_tr_b16 v[76:77], v182 offset:0x2500
	ds_read_b64_tr_b16 v[222:223], v182 offset:0x3400
	ds_read_b64_tr_b16 v[224:225], v182 offset:0x3500
	v_mfma_f32_32x32x16_bf16 v[32:47], v[218:221], v[104:107], v[32:47]
	s_waitcnt lgkmcnt(0)
	v_max_f32_e32 v64, v64, v65
	v_mfma_f32_32x32x16_bf16 v[16:31], v[66:69], v[96:99], v[16:31]
	v_cmp_ge_f32_e32 vcc, s26, v64
	s_cmp_eq_u64 vcc, exec
	v_mfma_f32_32x32x16_bf16 v[16:31], v[70:73], v[108:111], v[16:31]
	v_mfma_f32_32x32x16_bf16 v[16:31], v[74:77], v[100:103], v[16:31]
	v_mfma_f32_32x32x16_bf16 v[16:31], v[222:225], v[104:107], v[16:31]
	s_cbranch_scc0 .LBB4_810
	v_mov_b32_e32 v180, 1.0

; #define AT_SBAR() __builtin_amdgcn_sched_barrier(0)
; template <int OFF> DI s16x4 tr_read(int vb) { s16x4 r; asm volatile("ds_read_b64_tr_b16 %0, %1 offset:%2" : "=&v"(r) : "v"(vb), "i"(OFF) : "memory"); return r; }
; template <int D0> DI void pv_one(f32x16& od, int vb, bf16x8 pa0, bf16x8 pa1, bf16x8 pa2, bf16x8 pa3) {
;     const s16x4 l0 = tr_read<v_rd_off(D0, 0, 0)>(vb), h0 = tr_read<v_rd_off(D0, 0, 1)>(vb), l1 = tr_read<v_rd_off(D0, 1, 0)>(vb), h1 = tr_read<v_rd_off(D0, 1, 1)>(vb);
;     const s16x4 l2 = tr_read<v_rd_off(D0, 2, 0)>(vb), h2 = tr_read<v_rd_off(D0, 2, 1)>(vb), l3 = tr_read<v_rd_off(D0, 3, 0)>(vb), h3 = tr_read<v_rd_off(D0, 3, 1)>(vb);
;     asm volatile("s_waitcnt lgkmcnt(0)" ::: "memory"); AT_SBAR();
;     ...
;     od = __builtin_amdgcn_mfma_f32_32x32x16_bf16(AT_PK(l0, h0), pa0, od, 0, 0, 0);
;     od = __builtin_amdgcn_mfma_f32_32x32x16_bf16(AT_PK(l1, h1), pa1, od, 0, 0, 0);
;     od = __builtin_amdgcn_mfma_f32_32x32x16_bf16(AT_PK(l2, h2), pa2, od, 0, 0, 0);
;     od = __builtin_amdgcn_mfma_f32_32x32x16_bf16(AT_PK(l3, h3), pa3, od, 0, 0, 0);
;     ...
; }
; DI void pv_all_sm(f32x16* o, int vb, bf16x8 pa0, bf16x8 pa1, bf16x8 pa2, bf16x8 pa3, f32x16& p0, f32x16& p1, float& m_ref, f32x16& negm, float& alpha) {
;     pv_one<0>(o[0], vb, pa0, pa1, pa2, pa3);
;     float pmax = p0[0];
; #pragma unroll
;     for (int r = 1; r < 16; ++r) pmax = fmaxf(pmax, p0[r]);
;     pv_one<1>(o[1], vb, pa0, pa1, pa2, pa3);
; #pragma unroll
;     for (int r = 0; r < 16; ++r) pmax = fmaxf(pmax, p1[r]);
;     { auto rr = __builtin_amdgcn_permlane32_swap(__float_as_uint(pmax), __float_as_uint(pmax), false, false); pmax = fmaxf(__uint_as_float(rr[0]), __uint_as_float(rr[1])); }
;     pv_one<2>(o[2], vb, pa0, pa1, pa2, pa3);
;     alpha = 1.f;
;     if (__builtin_expect(!__all(pmax <= THRL), 0)) {
;         const float dl = fmaxf(pmax, 0.f); m_ref += dl; alpha = __builtin_amdgcn_exp2f(-dl);
; #pragma unroll
;         for (int r = 0; r < 16; ++r) { p0[r] -= dl; p1[r] -= dl; }
; #pragma unroll
;         for (int r = 0; r < 16; ++r) negm[r] = -m_ref;
;     }
.LBB4_798:
	v_lshl_add_u32 v219, s30, 14, v253
	ds_read_b64_tr_b16 v[220:221], v219 offset:0
	ds_read_b64_tr_b16 v[222:223], v219 offset:0x100
	ds_read_b64_tr_b16 v[224:225], v219 offset:0x1000
	ds_read_b64_tr_b16 v[226:227], v219 offset:0x1100
	ds_read_b64_tr_b16 v[228:229], v219 offset:0x2000
	ds_read_b64_tr_b16 v[230:231], v219 offset:0x2100
	ds_read_b64_tr_b16 v[232:233], v219 offset:0x3000
	ds_read_b64_tr_b16 v[234:235], v219 offset:0x3100
	s_waitcnt lgkmcnt(0)
	s_nop 0
	v_mfma_f32_32x32x16_bf16 v[48:63], v[220:223], v[120:123], v[48:63]
	v_max_f32_e32 v182, v128, v129
	ds_read_b64_tr_b16 v[220:221], v219 offset:0x200
	ds_read_b64_tr_b16 v[222:223], v219 offset:0x300
	v_max3_f32 v182, v182, v130, v131
	v_max3_f32 v182, v182, v132, v133
	v_mfma_f32_32x32x16_bf16 v[48:63], v[224:227], v[124:127], v[48:63]
	ds_read_b64_tr_b16 v[224:225], v219 offset:0x1200
	ds_read_b64_tr_b16 v[226:227], v219 offset:0x1300
	v_max3_f32 v182, v182, v134, v135
	v_max3_f32 v182, v182, v136, v137
	v_max3_f32 v182, v182, v138, v139
	v_max3_f32 v182, v182, v140, v141
	v_max3_f32 v182, v182, v142, v143
	v_mfma_f32_32x32x16_bf16 v[48:63], v[228:231], v[112:115], v[48:63]
	ds_read_b64_tr_b16 v[228:229], v219 offset:0x2200
	ds_read_b64_tr_b16 v[230:231], v219 offset:0x2300
	ds_read_b64_tr_b16 v[236:237], v219 offset:0x3200
	ds_read_b64_tr_b16 v[238:239], v219 offset:0x3300
	v_mfma_f32_32x32x16_bf16 v[48:63], v[232:235], v[116:119], v[48:63]
	s_waitcnt lgkmcnt(0)
	v_mfma_f32_32x32x16_bf16 v[32:47], v[220:223], v[120:123], v[32:47]
	v_max3_f32 v182, v182, v96, v97
	v_max3_f32 v182, v182, v98, v99
	ds_read_b64_tr_b16 v[222:223], v219 offset:0x400
	v_max3_f32 v182, v182, v100, v101
	v_max3_f32 v182, v182, v102, v103
	v_max3_f32 v182, v182, v104, v105
	v_max3_f32 v182, v182, v106, v107
	v_mfma_f32_32x32x16_bf16 v[32:47], v[224:227], v[124:127], v[32:47]
	ds_read_b64_tr_b16 v[224:225], v219 offset:0x500
	ds_read_b64_tr_b16 v[226:227], v219 offset:0x1400
	v_max3_f32 v182, v182, v108, v109
	v_max3_f32 v182, v182, v110, v111
	v_mov_b32_e32 v220, v182
	s_nop 1
	v_permlane32_swap_b32_e32 v182, v220
	v_mfma_f32_32x32x16_bf16 v[32:47], v[228:231], v[112:115], v[32:47]
	ds_read_b64_tr_b16 v[228:229], v219 offset:0x1500
	ds_read_b64_tr_b16 v[230:231], v219 offset:0x2400
	ds_read_b64_tr_b16 v[232:233], v219 offset:0x2500
	ds_read_b64_tr_b16 v[240:241], v219 offset:0x3400
	ds_read_b64_tr_b16 v[242:243], v219 offset:0x3500
	v_mfma_f32_32x32x16_bf16 v[32:47], v[236:239], v[116:119], v[32:47]
	s_waitcnt lgkmcnt(0)
	v_max_f32_e32 v220, v182, v220
	v_mfma_f32_32x32x16_bf16 v[16:31], v[222:225], v[120:123], v[16:31]
	v_cmp_ge_f32_e32 vcc, s26, v220
	s_cmp_eq_u64 vcc, exec
	v_mov_b32_e32 v182, 1.0
	v_mfma_f32_32x32x16_bf16 v[16:31], v[226:229], v[124:127], v[16:31]
	v_mfma_f32_32x32x16_bf16 v[16:31], v[230:233], v[112:115], v[16:31]
	v_mfma_f32_32x32x16_bf16 v[16:31], v[240:243], v[116:119], v[16:31]
	s_cbranch_scc0 .LBB4_811

; #define AT_SBAR() __builtin_amdgcn_sched_barrier(0)
; template <int OFF> DI s16x4 tr_read(int vb) { s16x4 r; asm volatile("ds_read_b64_tr_b16 %0, %1 offset:%2" : "=&v"(r) : "v"(vb), "i"(OFF) : "memory"); return r; }
; template <int D0> DI void pv_one(f32x16& od, int vb, bf16x8 pa0, bf16x8 pa1, bf16x8 pa2, bf16x8 pa3) {
;     const s16x4 l0 = tr_read<v_rd_off(D0, 0, 0)>(vb), h0 = tr_read<v_rd_off(D0, 0, 1)>(vb), l1 = tr_read<v_rd_off(D0, 1, 0)>(vb), h1 = tr_read<v_rd_off(D0, 1, 1)>(vb);
;     const s16x4 l2 = tr_read<v_rd_off(D0, 2, 0)>(vb), h2 = tr_read<v_rd_off(D0, 2, 1)>(vb), l3 = tr_read<v_rd_off(D0, 3, 0)>(vb), h3 = tr_read<v_rd_off(D0, 3, 1)>(vb);
;     asm volatile("s_waitcnt lgkmcnt(0)" ::: "memory"); AT_SBAR();
;     ...
;     od = __builtin_amdgcn_mfma_f32_32x32x16_bf16(AT_PK(l0, h0), pa0, od, 0, 0, 0);
;     od = __builtin_amdgcn_mfma_f32_32x32x16_bf16(AT_PK(l1, h1), pa1, od, 0, 0, 0);
;     od = __builtin_amdgcn_mfma_f32_32x32x16_bf16(AT_PK(l2, h2), pa2, od, 0, 0, 0);
;     od = __builtin_amdgcn_mfma_f32_32x32x16_bf16(AT_PK(l3, h3), pa3, od, 0, 0, 0);
;     ...
; }
; DI void pv_all_sm(f32x16* o, int vb, bf16x8 pa0, bf16x8 pa1, bf16x8 pa2, bf16x8 pa3, f32x16& p0, f32x16& p1, float& m_ref, f32x16& negm, float& alpha) {
;     pv_one<0>(o[0], vb, pa0, pa1, pa2, pa3);
;     float pmax = p0[0];
; #pragma unroll
;     for (int r = 1; r < 16; ++r) pmax = fmaxf(pmax, p0[r]);
;     pv_one<1>(o[1], vb, pa0, pa1, pa2, pa3);
; #pragma unroll
;     for (int r = 0; r < 16; ++r) pmax = fmaxf(pmax, p1[r]);
;     { auto rr = __builtin_amdgcn_permlane32_swap(__float_as_uint(pmax), __float_as_uint(pmax), false, false); pmax = fmaxf(__uint_as_float(rr[0]), __uint_as_float(rr[1])); }
;     pv_one<2>(o[2], vb, pa0, pa1, pa2, pa3);
;     alpha = 1.f;
;     if (__builtin_expect(!__all(pmax <= THRL), 0)) {
;         const float dl = fmaxf(pmax, 0.f); m_ref += dl; alpha = __builtin_amdgcn_exp2f(-dl);
; #pragma unroll
;         for (int r = 0; r < 16; ++r) { p0[r] -= dl; p1[r] -= dl; }
; #pragma unroll
;         for (int r = 0; r < 16; ++r) negm[r] = -m_ref;
;     }
.LBB4_851:
	s_lshl_b32 s65, s63, 14
	v_add_u32_e32 v182, s65, v253
	ds_read_b64_tr_b16 v[64:65], v182 offset:0
	ds_read_b64_tr_b16 v[66:67], v182 offset:0x100
	ds_read_b64_tr_b16 v[68:69], v182 offset:0x1000
	ds_read_b64_tr_b16 v[70:71], v182 offset:0x1100
	ds_read_b64_tr_b16 v[72:73], v182 offset:0x2000
	ds_read_b64_tr_b16 v[74:75], v182 offset:0x2100
	ds_read_b64_tr_b16 v[76:77], v182 offset:0x3000
	ds_read_b64_tr_b16 v[78:79], v182 offset:0x3100
	s_waitcnt lgkmcnt(0)
	s_nop 0
	v_mfma_f32_32x32x16_bf16 v[32:47], v[64:67], v[96:99], v[32:47]
	v_max_f32_e32 v64, v128, v129
	v_max3_f32 v64, v64, v130, v131
	v_max3_f32 v64, v64, v132, v133
	v_max3_f32 v64, v64, v134, v135
	v_max3_f32 v64, v64, v136, v137
	v_mfma_f32_32x32x16_bf16 v[32:47], v[68:71], v[108:111], v[32:47]
	v_max3_f32 v64, v64, v138, v139
	v_max3_f32 v66, v64, v140, v141
	ds_read_b64_tr_b16 v[64:65], v182 offset:0x200
	v_max3_f32 v180, v66, v142, v143
	ds_read_b64_tr_b16 v[66:67], v182 offset:0x300
	ds_read_b64_tr_b16 v[68:69], v182 offset:0x1200
	ds_read_b64_tr_b16 v[70:71], v182 offset:0x1300
	v_mfma_f32_32x32x16_bf16 v[32:47], v[72:75], v[100:103], v[32:47]
	ds_read_b64_tr_b16 v[72:73], v182 offset:0x2200
	ds_read_b64_tr_b16 v[74:75], v182 offset:0x2300
	ds_read_b64_tr_b16 v[214:215], v182 offset:0x3200
	ds_read_b64_tr_b16 v[216:217], v182 offset:0x3300
	v_mfma_f32_32x32x16_bf16 v[32:47], v[76:79], v[104:107], v[32:47]
	s_waitcnt lgkmcnt(0)
	v_mfma_f32_32x32x16_bf16 v[48:63], v[64:67], v[96:99], v[48:63]
	v_max3_f32 v76, v180, v112, v113
	v_max3_f32 v64, v76, v114, v115
	ds_read_b64_tr_b16 v[66:67], v182 offset:0x400
	v_max3_f32 v64, v64, v116, v117
	v_max3_f32 v64, v64, v118, v119
	v_max3_f32 v64, v64, v120, v121
	v_max3_f32 v64, v64, v122, v123
	v_mfma_f32_32x32x16_bf16 v[48:63], v[68:71], v[108:111], v[48:63]
	ds_read_b64_tr_b16 v[68:69], v182 offset:0x500
	ds_read_b64_tr_b16 v[70:71], v182 offset:0x1400
	v_max3_f32 v64, v64, v124, v125
	v_max3_f32 v64, v64, v126, v127
	v_mov_b32_e32 v65, v64
	s_nop 1
	v_permlane32_swap_b32_e32 v64, v65
	v_mfma_f32_32x32x16_bf16 v[48:63], v[72:75], v[100:103], v[48:63]
	ds_read_b64_tr_b16 v[72:73], v182 offset:0x1500
	ds_read_b64_tr_b16 v[74:75], v182 offset:0x2400
	ds_read_b64_tr_b16 v[76:77], v182 offset:0x2500
	ds_read_b64_tr_b16 v[218:219], v182 offset:0x3400
	ds_read_b64_tr_b16 v[220:221], v182 offset:0x3500
	v_mfma_f32_32x32x16_bf16 v[48:63], v[214:217], v[104:107], v[48:63]
	s_waitcnt lgkmcnt(0)
	v_max_f32_e32 v64, v64, v65
	v_mfma_f32_32x32x16_bf16 v[16:31], v[66:69], v[96:99], v[16:31]
	v_cmp_ge_f32_e32 vcc, s15, v64
	s_cmp_eq_u64 vcc, exec
	v_mfma_f32_32x32x16_bf16 v[16:31], v[70:73], v[108:111], v[16:31]
	v_mfma_f32_32x32x16_bf16 v[16:31], v[74:77], v[100:103], v[16:31]
	v_mfma_f32_32x32x16_bf16 v[16:31], v[218:221], v[104:107], v[16:31]
	s_cbranch_scc0 .LBB4_884
	v_mov_b32_e32 v180, 1.0

; #define AT_SBAR() __builtin_amdgcn_sched_barrier(0)
; template <int OFF> DI s16x4 tr_read(int vb) { s16x4 r; asm volatile("ds_read_b64_tr_b16 %0, %1 offset:%2" : "=&v"(r) : "v"(vb), "i"(OFF) : "memory"); return r; }
; template <int D0> DI void pv_one(f32x16& od, int vb, bf16x8 pa0, bf16x8 pa1, bf16x8 pa2, bf16x8 pa3) {
;     const s16x4 l0 = tr_read<v_rd_off(D0, 0, 0)>(vb), h0 = tr_read<v_rd_off(D0, 0, 1)>(vb), l1 = tr_read<v_rd_off(D0, 1, 0)>(vb), h1 = tr_read<v_rd_off(D0, 1, 1)>(vb);
;     const s16x4 l2 = tr_read<v_rd_off(D0, 2, 0)>(vb), h2 = tr_read<v_rd_off(D0, 2, 1)>(vb), l3 = tr_read<v_rd_off(D0, 3, 0)>(vb), h3 = tr_read<v_rd_off(D0, 3, 1)>(vb);
;     asm volatile("s_waitcnt lgkmcnt(0)" ::: "memory"); AT_SBAR();
;     ...
;     od = __builtin_amdgcn_mfma_f32_32x32x16_bf16(AT_PK(l0, h0), pa0, od, 0, 0, 0);
;     od = __builtin_amdgcn_mfma_f32_32x32x16_bf16(AT_PK(l1, h1), pa1, od, 0, 0, 0);
;     od = __builtin_amdgcn_mfma_f32_32x32x16_bf16(AT_PK(l2, h2), pa2, od, 0, 0, 0);
;     od = __builtin_amdgcn_mfma_f32_32x32x16_bf16(AT_PK(l3, h3), pa3, od, 0, 0, 0);
;     ...
; }
; DI void pv_all_sm(f32x16* o, int vb, bf16x8 pa0, bf16x8 pa1, bf16x8 pa2, bf16x8 pa3, f32x16& p0, f32x16& p1, float& m_ref, f32x16& negm, float& alpha) {
;     pv_one<0>(o[0], vb, pa0, pa1, pa2, pa3);
;     float pmax = p0[0];
; #pragma unroll
;     for (int r = 1; r < 16; ++r) pmax = fmaxf(pmax, p0[r]);
;     pv_one<1>(o[1], vb, pa0, pa1, pa2, pa3);
; #pragma unroll
;     for (int r = 0; r < 16; ++r) pmax = fmaxf(pmax, p1[r]);
;     { auto rr = __builtin_amdgcn_permlane32_swap(__float_as_uint(pmax), __float_as_uint(pmax), false, false); pmax = fmaxf(__uint_as_float(rr[0]), __uint_as_float(rr[1])); }
;     pv_one<2>(o[2], vb, pa0, pa1, pa2, pa3);
;     alpha = 1.f;
;     if (__builtin_expect(!__all(pmax <= THRL), 0)) {
;         const float dl = fmaxf(pmax, 0.f); m_ref += dl; alpha = __builtin_amdgcn_exp2f(-dl);
; #pragma unroll
;         for (int r = 0; r < 16; ++r) { p0[r] -= dl; p1[r] -= dl; }
; #pragma unroll
;         for (int r = 0; r < 16; ++r) negm[r] = -m_ref;
;     }
.LBB4_872:
	v_lshl_add_u32 v215, s64, 14, v253
	ds_read_b64_tr_b16 v[216:217], v215 offset:0
	ds_read_b64_tr_b16 v[218:219], v215 offset:0x100
	ds_read_b64_tr_b16 v[220:221], v215 offset:0x1000
	ds_read_b64_tr_b16 v[222:223], v215 offset:0x1100
	ds_read_b64_tr_b16 v[224:225], v215 offset:0x2000
	ds_read_b64_tr_b16 v[226:227], v215 offset:0x2100
	ds_read_b64_tr_b16 v[228:229], v215 offset:0x3000
	ds_read_b64_tr_b16 v[230:231], v215 offset:0x3100
	s_waitcnt lgkmcnt(0)
	s_nop 0
	v_mfma_f32_32x32x16_bf16 v[32:47], v[216:219], v[120:123], v[32:47]
	v_max_f32_e32 v182, v128, v129
	ds_read_b64_tr_b16 v[216:217], v215 offset:0x200
	ds_read_b64_tr_b16 v[218:219], v215 offset:0x300
	v_max3_f32 v182, v182, v130, v131
	v_max3_f32 v182, v182, v132, v133
	v_mfma_f32_32x32x16_bf16 v[32:47], v[220:223], v[124:127], v[32:47]
	ds_read_b64_tr_b16 v[220:221], v215 offset:0x1200
	ds_read_b64_tr_b16 v[222:223], v215 offset:0x1300
	v_max3_f32 v182, v182, v134, v135
	v_max3_f32 v182, v182, v136, v137
	v_max3_f32 v182, v182, v138, v139
	v_max3_f32 v182, v182, v140, v141
	v_max3_f32 v182, v182, v142, v143
	v_mfma_f32_32x32x16_bf16 v[32:47], v[224:227], v[112:115], v[32:47]
	ds_read_b64_tr_b16 v[224:225], v215 offset:0x2200
	ds_read_b64_tr_b16 v[226:227], v215 offset:0x2300
	ds_read_b64_tr_b16 v[232:233], v215 offset:0x3200
	ds_read_b64_tr_b16 v[234:235], v215 offset:0x3300
	v_mfma_f32_32x32x16_bf16 v[32:47], v[228:231], v[116:119], v[32:47]
	s_waitcnt lgkmcnt(0)
	v_mfma_f32_32x32x16_bf16 v[48:63], v[216:219], v[120:123], v[48:63]
	v_max3_f32 v182, v182, v96, v97
	v_max3_f32 v182, v182, v98, v99
	ds_read_b64_tr_b16 v[218:219], v215 offset:0x400
	v_max3_f32 v182, v182, v100, v101
	v_max3_f32 v182, v182, v102, v103
	v_max3_f32 v182, v182, v104, v105
	v_max3_f32 v182, v182, v106, v107
	v_mfma_f32_32x32x16_bf16 v[48:63], v[220:223], v[124:127], v[48:63]
	ds_read_b64_tr_b16 v[220:221], v215 offset:0x500
	ds_read_b64_tr_b16 v[222:223], v215 offset:0x1400
	v_max3_f32 v182, v182, v108, v109
	v_max3_f32 v182, v182, v110, v111
	v_mov_b32_e32 v216, v182
	s_nop 1
	v_permlane32_swap_b32_e32 v182, v216
	v_mfma_f32_32x32x16_bf16 v[48:63], v[224:227], v[112:115], v[48:63]
	ds_read_b64_tr_b16 v[224:225], v215 offset:0x1500
	ds_read_b64_tr_b16 v[226:227], v215 offset:0x2400
	ds_read_b64_tr_b16 v[228:229], v215 offset:0x2500
	ds_read_b64_tr_b16 v[236:237], v215 offset:0x3400
	ds_read_b64_tr_b16 v[238:239], v215 offset:0x3500
	v_mfma_f32_32x32x16_bf16 v[48:63], v[232:235], v[116:119], v[48:63]
	s_waitcnt lgkmcnt(0)
	v_max_f32_e32 v216, v182, v216
	v_mfma_f32_32x32x16_bf16 v[16:31], v[218:221], v[120:123], v[16:31]
	v_cmp_ge_f32_e32 vcc, s15, v216
	s_cmp_eq_u64 vcc, exec
	v_mov_b32_e32 v182, 1.0
	v_mfma_f32_32x32x16_bf16 v[16:31], v[222:225], v[124:127], v[16:31]
	v_mfma_f32_32x32x16_bf16 v[16:31], v[226:229], v[112:115], v[16:31]
	v_mfma_f32_32x32x16_bf16 v[16:31], v[236:239], v[116:119], v[16:31]
	s_cbranch_scc0 .LBB4_885
